# PEER table conversion (HBM-bound bulk of phase 7) runs inside phase 8: half of the workgroups convert before their score-GEMM units, half after; phase 7 keeps only csh
# speedup vs baseline: 1.0113x; 1.0034x over previous
.LBB0_869:
	s_cmp_lt_i32 s40, 8
	s_cselect_b64 s[2:3], -1, 0
	s_cmp_gt_i32 s41, 7
	s_cselect_b64 s[4:5], -1, 0
	s_and_b64 s[10:11], s[2:3], s[4:5]
	s_andn2_b64 vcc, exec, s[10:11]
	s_cbranch_vccnz .LBB0_911
	s_mov_b32 s93, 0
	s_mov_b32 s95, 1

.LBB0_873:
	s_or_b64 exec, exec, s[2:3]
	s_lshl_b32 s2, s24, 3
	s_ashr_i32 s3, s16, 6
	v_and_b32_e32 v131, 63, v130
	s_add_i32 s16, s3, s2
	s_lshl_b32 s18, s17, 3
	s_cmpk_gt_i32 s16, 0x7ff
	v_cmp_eq_u32_e64 s[2:3], 0, v131
	s_waitcnt lgkmcnt(0)
	s_barrier
	s_cbranch_scc1 .LBB0_884
	s_cmp_eq_u32 s93, 1
	s_cbranch_scc1 .LBB0_884
	v_lshl_add_u32 v124, v131, 5, 0
	ds_read_b128 v[0:3], v124
	ds_read_b128 v[4:7], v124 offset:16
	ds_read_b128 v[8:11], v124 offset:8192
	ds_read_b128 v[12:15], v124 offset:8208
	ds_read_b128 v[16:19], v124 offset:16384
	ds_read_b128 v[20:23], v124 offset:16400
	ds_read_b128 v[24:27], v124 offset:24576
	ds_read_b128 v[28:31], v124 offset:24592
	ds_read_b128 v[32:35], v124 offset:2048
	ds_read_b128 v[36:39], v124 offset:2064
	ds_read_b128 v[40:43], v124 offset:10240
	ds_read_b128 v[44:47], v124 offset:10256
	ds_read_b128 v[48:51], v124 offset:18432
	ds_read_b128 v[52:55], v124 offset:18448
	ds_read_b128 v[56:59], v124 offset:26624
	ds_read_b128 v[60:63], v124 offset:26640
	ds_read_b128 v[64:67], v124 offset:4096
	ds_read_b128 v[68:71], v124 offset:4112
	ds_read_b128 v[72:75], v124 offset:12288
	ds_read_b128 v[76:79], v124 offset:12304
	ds_read_b128 v[80:83], v124 offset:20480
	ds_read_b128 v[84:87], v124 offset:20496
	ds_read_b128 v[88:91], v124 offset:28672
	ds_read_b128 v[92:95], v124 offset:28688
	ds_read_b128 v[96:99], v124 offset:6144
	ds_read_b128 v[100:103], v124 offset:6160
	ds_read_b128 v[104:107], v124 offset:14336
	ds_read_b128 v[108:111], v124 offset:14352
	ds_read_b128 v[112:115], v124 offset:22528
	ds_read_b128 v[116:119], v124 offset:22544
	ds_read_b128 v[120:123], v124 offset:30720
	ds_read_b128 v[124:127], v124 offset:30736
	s_ashr_i32 s17, s16, 31
	s_ashr_i32 s19, s18, 31
	s_lshl_b64 s[20:21], s[16:17], 12
	s_lshl_b64 s[6:7], s[16:17], 2
	s_lshl_b64 s[8:9], s[18:19], 2
	v_lshl_or_b32 v128, v131, 4, s20
	v_mov_b32_e32 v129, s21
	s_lshl_b64 s[20:21], s[18:19], 12
	v_mov_b32_e32 v132, 0x3d80000
	v_mov_b32_e32 v133, 0x3d82000
	v_mov_b32_e32 v134, 0x3d84000
	v_mov_b32_e32 v135, 0x3d86000
	s_mov_b32 s17, s16
	s_branch .LBB0_876

.LBB0_884:
	s_cmp_eq_u32 s93, 0
	s_cbranch_scc1 .Lp7_exit
	s_cmpk_lt_i32 s16, 0x1000
	s_movk_i32 s17, 0x1000
	s_cbranch_scc0 .Lp7_exit
	s_add_u32 s19, s4, 0x4000000
	s_addc_u32 s33, s5, 0
	s_add_u32 s38, s4, 0x6000000
	s_addc_u32 s39, s5, 0
	s_add_u32 s20, s4, 0x3e00000
	s_addc_u32 s21, s5, 0
	s_lshl_b32 s36, s16, 3
	s_add_i32 s2, s36, 0xffffc000
	s_ashr_i32 s3, s36, 31
	s_cmpk_gt_i32 s16, 0x7ff
	s_cselect_b32 s3, 0, s3
	s_cselect_b32 s2, s2, s36
	s_cselect_b32 s4, s15, s13
	s_cselect_b32 s5, s14, s12
	s_lshl_b64 s[2:3], s[2:3], 13
	s_add_u32 s2, s5, s2
	v_mov_b32_e32 v161, 0
	s_addc_u32 s3, s4, s3
	v_lshlrev_b32_e32 v160, 4, v131
	v_lshl_add_u64 v[0:1], s[2:3], 0, v[160:161]
	v_add_co_u32_e32 v32, vcc, s17, v0
	s_mov_b32 s42, 2
	s_nop 0
	v_addc_co_u32_e32 v33, vcc, 0, v1, vcc
	global_load_dwordx4 v[0:3], v[32:33], off offset:3072 nt
	global_load_dwordx4 v[4:7], v[32:33], off offset:2048 nt
	global_load_dwordx4 v[8:11], v[32:33], off offset:1024 nt
	global_load_dwordx4 v[16:19], v[32:33], off nt
	global_load_dwordx4 v[12:15], v160, s[2:3] offset:3072 nt
	global_load_dwordx4 v[20:23], v160, s[2:3] offset:2048 nt
	global_load_dwordx4 v[24:27], v160, s[2:3] offset:1024 nt
	global_load_dwordx4 v[28:31], v160, s[2:3] nt
	v_and_b32_e32 v32, 16, v130
	v_cmp_eq_u32_e64 s[2:3], 0, v32
	v_lshlrev_b32_e32 v32, 2, v130
	v_and_b32_e32 v164, 0x7c, v32
	v_lshlrev_b32_e32 v32, 9, v131
	v_and_b32_e32 v168, 0x4000, v32
	v_lshlrev_b32_e32 v162, 2, v131
	s_mov_b32 s34, 0
	v_cmp_gt_u32_e64 s[4:5], 32, v131
	v_mov_b32_e32 v165, v161
	v_cmp_gt_u32_e64 s[6:7], 4, v131
	v_lshlrev_b32_e32 v166, 14, v131
	v_mov_b32_e32 v167, v161
	v_add_u32_e32 v163, 0, v160
	v_cmp_eq_u32_e64 s[8:9], 0, v131
	v_mov_b32_e32 v169, v161
	v_or_b32_e32 v170, 0x8000, v168
	v_mov_b32_e32 v171, v161
	v_or_b32_e32 v172, 0x10000, v168
	v_mov_b32_e32 v173, v161
	v_or_b32_e32 v174, 0x18000, v168
	v_mov_b32_e32 v175, v161
	v_or_b32_e32 v176, 0x20000, v168
	v_mov_b32_e32 v177, v161
	v_or_b32_e32 v178, 0x28000, v168
	v_mov_b32_e32 v179, v161
	v_or_b32_e32 v180, 0x30000, v168
	v_mov_b32_e32 v181, v161
	v_or_b32_e32 v182, 0x38000, v168
	v_mov_b32_e32 v183, v161
	v_mov_b32_e32 v184, 0x40000
	v_mov_b32_e32 v185, 0x80000
	v_mov_b32_e32 v186, 0xc0000
	v_mov_b32_e32 v187, 0xe3
	v_mov_b32_e32 v188, 0x3800000
	s_mov_b32 s35, s36
	s_branch .LBB0_888

.Lp7_exit:
	s_cmp_eq_u32 s95, 2
	s_cbranch_scc1 .Lp7_retA
	s_cmp_eq_u32 s95, 3
	s_cbranch_scc1 .Lp7_retC
	s_branch .LBB0_911
.Lp7_retA:
	s_waitcnt vmcnt(0) lgkmcnt(0)
	s_barrier
	s_mov_b64 s[42:43], s[96:97]
	s_mov_b32 s95, 4
	s_branch .Lp8_body
.Lp7_retC:
	s_waitcnt vmcnt(0) lgkmcnt(0)
	s_mov_b64 s[42:43], s[96:97]
	s_mov_b32 s95, 4
	s_branch .Lp8_done

.LBB0_965:
	s_cmp_lt_i32 s40, 9
	s_cselect_b64 s[4:5], -1, 0
	s_and_b64 s[42:43], s[4:5], s[2:3]
	s_andn2_b64 vcc, exec, s[42:43]
	s_cbranch_vccnz .LBB0_994
	s_lshr_b32 s94, s24, 3
	s_and_b32 s94, s94, 1
	s_cmp_eq_u32 s94, 0
	s_cbranch_scc0 .Lp8_body
	s_mov_b64 s[96:97], s[42:43]
	s_mov_b32 s93, 1
	s_mov_b32 s95, 2
	s_branch .Lp7_body
.Lp8_body:
	s_waitcnt vmcnt(0)
	v_mbcnt_lo_u32_b32 v0, -1, 0
	v_mbcnt_hi_u32_b32 v0, -1, v0
	s_mov_b64 s[2:3], s[0:1]
	v_or_b32_e32 v153, s25, v0
	v_bfe_i32 v4, v153, 27, 1
	s_waitcnt lgkmcnt(0)
	v_lshlrev_b32_e32 v1, 4, v153
	v_lshrrev_b32_e32 v4, 22, v4
	v_add_u32_e32 v4, v1, v4
	v_and_b32_e32 v4, 0xfffffc00, v4
	v_sub_u32_e32 v4, v1, v4
	v_lshrrev_b32_e32 v5, 4, v4
	v_bitop3_b32 v4, v5, v4, 32 bitop3:0x6c
	v_ashrrev_i32_e32 v6, 31, v4
	v_ashrrev_i32_e32 v2, 31, v153
	v_lshrrev_b32_e32 v6, 26, v6
	v_lshrrev_b32_e32 v2, 26, v2
	v_add_u32_e32 v6, v4, v6
	v_add_u32_e32 v2, v153, v2
	v_ashrrev_i32_e32 v7, 6, v6
	v_and_b32_e32 v6, 0xc0, v6
	v_ashrrev_i32_e32 v3, 6, v2
	v_sub_u32_e32 v4, v4, v6
	v_mov_b32_e32 v6, 1
	v_lshlrev_b32_e32 v5, 3, v3
	v_lshlrev_b32_e32 v8, 5, v3
	v_ashrrev_i16_sdwa v4, v6, sext(v4) dst_sel:DWORD dst_unused:UNUSED_PAD src0_sel:DWORD src1_sel:BYTE_0
	v_and_b32_e32 v5, -16, v5
	v_and_b32_e32 v8, 32, v8
	v_bfe_i32 v4, v4, 0, 16
	s_load_dword s33, s[0:1], 0xc8
	s_load_dwordx2 s[44:45], s[2:3], 0xb8
	v_add_u32_e32 v5, v7, v5
	v_and_b32_e32 v11, 3, v7
	s_mov_b32 s2, 0xfffe0
	v_add_lshl_u32 v8, v8, v4, 1
	v_add_u32_e32 v1, 0x2000, v1
	v_lshlrev_b32_e32 v9, 1, v5
	v_lshrrev_b32_e32 v10, 2, v5
	v_and_or_b32 v11, v5, s2, v11
	v_lshl_add_u32 v144, v5, 12, v8
	v_ashrrev_i32_e32 v5, 31, v1
	v_lshrrev_b32_e32 v5, 22, v5
	v_and_b32_e32 v9, 24, v9
	v_and_b32_e32 v10, 4, v10
	v_add_u32_e32 v5, v1, v5
	v_or3_b32 v9, v11, v10, v9
	v_ashrrev_i32_e32 v5, 10, v5
	v_lshl_add_u32 v146, v9, 12, v8
	v_mul_i32_i24_e32 v8, 0x400, v5
	s_ashr_i32 s60, s24, 31
	s_waitcnt lgkmcnt(0)
	s_ashr_i32 s61, s33, 31
	v_sub_u32_e32 v1, v1, v8
	s_add_u32 s62, s44, 0xa4000
	v_lshrrev_b32_e32 v8, 4, v1
	s_addc_u32 s63, s45, 0
	v_bitop3_b32 v1, v8, v1, 32 bitop3:0x6c
	s_add_u32 s64, s44, 0x8000000
	v_ashrrev_i32_e32 v9, 31, v1
	v_lshlrev_b32_e32 v3, 15, v3
	s_addc_u32 s65, s45, 0
	v_lshrrev_b32_e32 v9, 26, v9
	v_and_b32_e32 v3, 0xffff0000, v3
	s_add_u32 s66, s44, 0x1e00000
	v_lshlrev_b32_e32 v8, 3, v5
	v_add_u32_e32 v9, v1, v9
	v_lshl_add_u32 v3, v7, 12, v3
	s_addc_u32 s67, s45, 0
	v_and_b32_e32 v8, -16, v8
	v_ashrrev_i32_e32 v10, 6, v9
	v_and_or_b32 v2, v2, 64, v3
	s_add_u32 s46, s44, 0x3400000
	v_add_u32_e32 v8, v10, v8
	v_and_b32_e32 v9, 0xc0, v9
	v_and_b32_e32 v12, 3, v10
	v_mov_b32_e32 v155, 0
	v_lshl_add_u32 v154, v4, 1, v2
	s_addc_u32 s47, s45, 0
	v_sub_u32_e32 v1, v1, v9
	v_and_or_b32 v12, v8, s2, v12
	v_lshl_add_u64 v[2:3], s[44:45], 0, v[154:155]
	s_mov_b64 s[2:3], 0x8080080
	s_add_u32 s48, s44, 0x2c00000
	v_lshlrev_b32_e32 v11, 5, v5
	v_ashrrev_i16_sdwa v1, v6, sext(v1) dst_sel:DWORD dst_unused:UNUSED_PAD src0_sel:DWORD src1_sel:BYTE_0
	v_lshlrev_b32_e32 v6, 1, v8
	v_lshrrev_b32_e32 v9, 2, v8
	v_lshl_add_u64 v[156:157], v[2:3], 0, s[2:3]
	v_lshlrev_b32_e32 v2, 15, v5
	s_addc_u32 s49, s45, 0
	v_and_b32_e32 v11, 32, v11
	v_bfe_i32 v1, v1, 0, 16
	v_and_b32_e32 v6, 24, v6
	v_and_b32_e32 v9, 4, v9
	v_and_b32_e32 v2, 0xffff0000, v2
	s_add_u32 s68, s44, 0x3d80000
	v_or3_b32 v6, v12, v9, v6
	v_add_lshl_u32 v9, v11, v1, 1
	v_lshl_add_u32 v2, v10, 12, v2
	v_lshlrev_b32_e32 v3, 6, v5
	s_addc_u32 s69, s45, 0
	v_lshl_add_u32 v150, v6, 12, v9
	v_and_b32_e32 v152, 15, v0
	v_bfe_u32 v6, v0, 4, 2
	v_lshlrev_b32_e32 v0, 2, v0
	v_and_or_b32 v2, v3, 64, v2
	s_add_u32 s50, s44, 0x18800000
	v_lshl_add_u32 v148, v8, 12, v9
	v_lshlrev_b32_e32 v8, 4, v6
	v_lshlrev_b32_e32 v9, 6, v152
	v_and_b32_e32 v0, 32, v0
	v_lshl_add_u32 v154, v1, 1, v2
	s_addc_u32 s51, s45, 0
	v_bitop3_b32 v166, v8, v0, v9 bitop3:0x36
	v_lshlrev_b32_e32 v0, 3, v6
	v_lshl_add_u64 v[2:3], s[44:45], 0, v[154:155]
	v_lshl_add_u64 v[158:159], v[2:3], 0, s[2:3]
	s_add_u32 s70, s44, 0x1e00100
	v_lshlrev_b32_e32 v168, 2, v0
	v_lshlrev_b32_e32 v0, 2, v152
	s_flbit_i32_b32 s2, 0
	v_mov_b32_e32 v147, v155
	v_mov_b32_e32 v151, v155
	v_mov_b32_e32 v145, v155
	v_mov_b32_e32 v149, v155
	s_mov_b32 s52, 0
	v_lshl_add_u32 v167, v6, 5, 0
	s_addc_u32 s71, s45, 0
	v_mov_b64_e32 v[160:161], 0x200
	v_mov_b64_e32 v[162:163], 0x1ff
	s_mov_b64 s[54:55], 0x80
	s_movk_i32 s72, 0x440
	v_mov_b32_e32 v169, 0x358637bd
	s_mov_b32 s73, 0x800000
	s_movk_i32 s74, 0xff00
	s_mov_b32 s75, 0xff61b1e6
	v_lshl_or_b32 v170, v152, 6, v8
	v_and_b32_e32 v171, 32, v0
	s_min_u32 s76, s2, 32
	s_mov_b32 s77, 0
	s_branch .LBB0_969

.LBB0_994:
	s_cmp_eq_u32 s94, 1
	s_cbranch_scc0 .Lp8_done
	s_cmp_eq_u32 s95, 4
	s_cbranch_scc1 .Lp8_done
	s_mov_b64 s[96:97], s[42:43]
	s_mov_b32 s93, 1
	s_mov_b32 s95, 3
	s_branch .Lp7_body

	.amdhsa_kernel _Z4mega4Args
		.amdhsa_group_segment_fixed_size 0
		.amdhsa_private_segment_fixed_size 0
		.amdhsa_kernarg_size 456
		.amdhsa_user_sgpr_count 2
		.amdhsa_user_sgpr_dispatch_ptr 0
		.amdhsa_user_sgpr_queue_ptr 0
		.amdhsa_user_sgpr_kernarg_segment_ptr 1
		.amdhsa_user_sgpr_dispatch_id 0
		.amdhsa_user_sgpr_kernarg_preload_length 0
		.amdhsa_user_sgpr_kernarg_preload_offset 0
		.amdhsa_user_sgpr_private_segment_size 0
		.amdhsa_uses_dynamic_stack 0
		.amdhsa_enable_private_segment 0
		.amdhsa_system_sgpr_workgroup_id_x 1
		.amdhsa_system_sgpr_workgroup_id_y 0
		.amdhsa_system_sgpr_workgroup_id_z 0
		.amdhsa_system_sgpr_workgroup_info 0
		.amdhsa_system_vgpr_workitem_id 0
		.amdhsa_next_free_vgpr 256
		.amdhsa_next_free_sgpr 98
		.amdhsa_accum_offset 256
		.amdhsa_reserve_vcc 1
		.amdhsa_float_round_mode_32 0
		.amdhsa_float_round_mode_16_64 0
		.amdhsa_float_denorm_mode_32 3
		.amdhsa_float_denorm_mode_16_64 3
		.amdhsa_dx10_clamp 1
		.amdhsa_ieee_mode 1
		.amdhsa_fp16_overflow 0
		.amdhsa_tg_split 0
		.amdhsa_exception_fp_ieee_invalid_op 0
		.amdhsa_exception_fp_denorm_src 0
		.amdhsa_exception_fp_ieee_div_zero 0
		.amdhsa_exception_fp_ieee_overflow 0
		.amdhsa_exception_fp_ieee_underflow 0
		.amdhsa_exception_fp_ieee_inexact 0
		.amdhsa_exception_int_div_zero 0
	.end_amdhsa_kernel

amdhsa.kernels:
  - .agpr_count:     0
    .args:
      - .offset:         0
        .size:           200
        .value_kind:     by_value
      - .offset:         200
        .size:           4
        .value_kind:     hidden_block_count_x
      - .offset:         204
        .size:           4
        .value_kind:     hidden_block_count_y
      - .offset:         208
        .size:           4
        .value_kind:     hidden_block_count_z
      - .offset:         212
        .size:           2
        .value_kind:     hidden_group_size_x
      - .offset:         214
        .size:           2
        .value_kind:     hidden_group_size_y
      - .offset:         216
        .size:           2
        .value_kind:     hidden_group_size_z
      - .offset:         218
        .size:           2
        .value_kind:     hidden_remainder_x
      - .offset:         220
        .size:           2
        .value_kind:     hidden_remainder_y
      - .offset:         222
        .size:           2
        .value_kind:     hidden_remainder_z
      - .offset:         240
        .size:           8
        .value_kind:     hidden_global_offset_x
      - .offset:         248
        .size:           8
        .value_kind:     hidden_global_offset_y
      - .offset:         256
        .size:           8
        .value_kind:     hidden_global_offset_z
      - .offset:         264
        .size:           2
        .value_kind:     hidden_grid_dims
      - .offset:         320
        .size:           4
        .value_kind:     hidden_dynamic_lds_size
    .group_segment_fixed_size: 0
    .kernarg_segment_align: 8
    .kernarg_segment_size: 456
    .language:       OpenCL C
    .language_version:
      - 2
      - 0
    .max_flat_workgroup_size: 512
    .name:           _Z4mega4Args
    .private_segment_fixed_size: 0
    .sgpr_count:     104
    .sgpr_spill_count: 0
    .symbol:         _Z4mega4Args.kd
    .uniform_work_group_size: 1
    .uses_dynamic_stack: false
    .vgpr_count:     256
    .vgpr_spill_count: 0
    .wavefront_size: 64
